# MoE phase start: both halves of the expert counter table are loaded in one batch (second wait removed)
# baseline (speedup 1.0000x reference)
.LBB0_1929:
	s_andn2_b64 vcc, exec, s[0:1]
	s_cbranch_vccnz .LBB0_2137
	v_readlane_b32 s0, v251, 1
	v_readlane_b32 s2, v251, 10
	v_readlane_b32 s1, v251, 2
	v_readlane_b32 s3, v251, 11
	s_load_dword s58, s[2:3], 0x0
	v_readlane_b32 s30, v251, 0
	s_load_dwordx2 s[2:3], s[0:1], 0x108
	v_readlane_b32 s4, v251, 12
	s_waitcnt lgkmcnt(0)
	s_mov_b32 s59, s58
	s_waitcnt vmcnt(7)
	v_mbcnt_lo_u32_b32 v18, -1, 0
	v_mbcnt_hi_u32_b32 v18, -1, v18
	s_nop 0
	v_add_u32_e32 v0, s4, v18
	v_cmp_eq_u32_e64 s[4:5], 0, v0
	s_and_saveexec_b64 s[6:7], s[4:5]
	s_cbranch_execz .LBB0_1932
	s_add_u32 s8, s2, 0x556ec800
	s_addc_u32 s9, s3, 0
	s_waitcnt vmcnt(6)
	v_mov_b32_e32 v24, 0x556ec000
	global_load_dwordx4 v[2:5], v1, s[8:9] offset:48
	global_load_dwordx4 v[6:9], v1, s[8:9] offset:32
	global_load_dwordx4 v[10:13], v1, s[8:9] offset:16
	global_load_dwordx4 v[14:17], v24, s[2:3] offset:2048
	global_load_dwordx4 v[56:59], v1, s[8:9] offset:112
	global_load_dwordx4 v[60:63], v1, s[8:9] offset:96
	global_load_dwordx4 v[64:67], v1, s[8:9] offset:80
	global_load_dwordx4 v[68:71], v24, s[2:3] offset:2112
	v_readlane_b32 s8, v252, 45
	v_readlane_b32 s10, v252, 58
	s_waitcnt vmcnt(0)
	v_add_u32_e32 v19, 0xff, v14
	v_add_u32_e32 v21, 0xff, v15
	v_ashrrev_i32_e32 v20, 31, v19
	v_ashrrev_i32_e32 v22, 31, v21
	v_add_u32_sdwa v19, v19, v20 dst_sel:DWORD dst_unused:UNUSED_PAD src0_sel:DWORD src1_sel:BYTE_3
	v_add_u32_sdwa v21, v21, v22 dst_sel:DWORD dst_unused:UNUSED_PAD src0_sel:DWORD src1_sel:BYTE_3
	v_ashrrev_i32_e32 v20, 8, v19
	v_ashrrev_i32_e32 v21, 8, v21
	v_add_u32_e32 v23, v21, v20
	v_lshlrev_b32_e32 v22, 8, v23
	v_and_b32_e32 v21, 0xffffff00, v19
	v_mov_b32_e32 v20, v1
	v_mov_b32_e32 v19, s8
	ds_write_b96 v19, v[20:22]
	v_add_u32_e32 v19, 0xff, v16
	v_ashrrev_i32_e32 v20, 31, v19
	s_add_i32 s8, 0, 0x20000
	v_add_u32_sdwa v19, v19, v20 dst_sel:DWORD dst_unused:UNUSED_PAD src0_sel:DWORD src1_sel:BYTE_3
	v_mov_b32_e32 v20, s8
	ds_write_b128 v20, v[14:17]
	v_add_u32_e32 v14, 0xff, v17
	v_ashrrev_i32_e32 v15, 31, v14
	v_ashrrev_i32_e32 v19, 8, v19
	v_add_u32_sdwa v14, v14, v15 dst_sel:DWORD dst_unused:UNUSED_PAD src0_sel:DWORD src1_sel:BYTE_3
	v_ashrrev_i32_e32 v14, 8, v14
	v_add_u32_e32 v15, v19, v23
	v_add_u32_e32 v19, v14, v15
	v_readlane_b32 s8, v252, 46
	v_lshlrev_b32_e32 v16, 8, v15
	v_lshlrev_b32_e32 v17, 8, v19
	v_mov_b32_e32 v14, v21
	v_mov_b32_e32 v15, v22
	v_mov_b32_e32 v20, s8
	v_readlane_b32 s8, v252, 47
	ds_write_b128 v20, v[14:17]
	s_nop 0
	v_mov_b32_e32 v14, s8
	ds_write2_b32 v14, v16, v17 offset1:1
	v_add_u32_e32 v14, 0xff, v10
	v_ashrrev_i32_e32 v15, 31, v14
	v_add_u32_sdwa v14, v14, v15 dst_sel:DWORD dst_unused:UNUSED_PAD src0_sel:DWORD src1_sel:BYTE_3
	v_add_u32_e32 v15, 0xff, v11
	v_ashrrev_i32_e32 v16, 31, v15
	v_ashrrev_i32_e32 v14, 8, v14
	v_add_u32_sdwa v15, v15, v16 dst_sel:DWORD dst_unused:UNUSED_PAD src0_sel:DWORD src1_sel:BYTE_3
	v_ashrrev_i32_e32 v15, 8, v15
	v_add_u32_e32 v14, v14, v19
	v_add_u32_e32 v16, v15, v14
	v_readlane_b32 s8, v252, 48
	v_lshlrev_b32_e32 v14, 8, v14
	v_lshlrev_b32_e32 v15, 8, v16
	v_mov_b32_e32 v17, s8
	ds_write2_b32 v17, v14, v15 offset1:1
	v_add_u32_e32 v17, 0xff, v12
	v_ashrrev_i32_e32 v19, 31, v17
	v_readlane_b32 s8, v252, 49
	v_add_u32_sdwa v17, v17, v19 dst_sel:DWORD dst_unused:UNUSED_PAD src0_sel:DWORD src1_sel:BYTE_3
	v_ashrrev_i32_e32 v17, 8, v17
	v_mov_b32_e32 v19, s8
	ds_write_b128 v19, v[10:13]
	v_add_u32_e32 v10, 0xff, v13
	v_ashrrev_i32_e32 v11, 31, v10
	v_add_u32_sdwa v10, v10, v11 dst_sel:DWORD dst_unused:UNUSED_PAD src0_sel:DWORD src1_sel:BYTE_3
	v_ashrrev_i32_e32 v10, 8, v10
	v_add_u32_e32 v11, v17, v16
	v_add_u32_e32 v10, v10, v11
	v_readlane_b32 s8, v252, 50
	v_lshlrev_b32_e32 v16, 8, v11
	v_lshlrev_b32_e32 v17, 8, v10
	v_mov_b32_e32 v11, s8
	v_readlane_b32 s8, v252, 51
	ds_write_b128 v11, v[14:17]
	s_nop 0
	v_mov_b32_e32 v11, s8
	ds_write2_b32 v11, v16, v17 offset1:1
	v_add_u32_e32 v11, 0xff, v6
	v_ashrrev_i32_e32 v12, 31, v11
	v_add_u32_sdwa v11, v11, v12 dst_sel:DWORD dst_unused:UNUSED_PAD src0_sel:DWORD src1_sel:BYTE_3
	v_add_u32_e32 v12, 0xff, v7
	v_ashrrev_i32_e32 v13, 31, v12
	v_ashrrev_i32_e32 v11, 8, v11
	v_add_u32_sdwa v12, v12, v13 dst_sel:DWORD dst_unused:UNUSED_PAD src0_sel:DWORD src1_sel:BYTE_3
	v_ashrrev_i32_e32 v12, 8, v12
	v_add_u32_e32 v10, v11, v10
	v_add_u32_e32 v12, v12, v10
	v_readlane_b32 s8, v252, 52
	v_lshlrev_b32_e32 v10, 8, v10
	v_lshlrev_b32_e32 v11, 8, v12
	v_mov_b32_e32 v13, s8
	ds_write2_b32 v13, v10, v11 offset1:1
	v_add_u32_e32 v13, 0xff, v8
	v_ashrrev_i32_e32 v14, 31, v13
	v_readlane_b32 s8, v252, 53
	v_add_u32_sdwa v13, v13, v14 dst_sel:DWORD dst_unused:UNUSED_PAD src0_sel:DWORD src1_sel:BYTE_3
	v_ashrrev_i32_e32 v13, 8, v13
	v_mov_b32_e32 v14, s8
	ds_write_b128 v14, v[6:9]
	v_add_u32_e32 v6, 0xff, v9
	v_ashrrev_i32_e32 v7, 31, v6
	v_add_u32_sdwa v6, v6, v7 dst_sel:DWORD dst_unused:UNUSED_PAD src0_sel:DWORD src1_sel:BYTE_3
	v_ashrrev_i32_e32 v6, 8, v6
	v_add_u32_e32 v7, v13, v12
	v_add_u32_e32 v6, v6, v7
	v_readlane_b32 s8, v252, 54
	v_lshlrev_b32_e32 v12, 8, v7
	v_lshlrev_b32_e32 v13, 8, v6
	v_mov_b32_e32 v7, s8
	v_readlane_b32 s8, v252, 55
	ds_write_b128 v7, v[10:13]
	s_nop 0
	v_mov_b32_e32 v7, s8
	ds_write2_b32 v7, v12, v13 offset1:1
	v_add_u32_e32 v7, 0xff, v2
	v_ashrrev_i32_e32 v8, 31, v7
	v_add_u32_sdwa v7, v7, v8 dst_sel:DWORD dst_unused:UNUSED_PAD src0_sel:DWORD src1_sel:BYTE_3
	v_add_u32_e32 v8, 0xff, v3
	v_ashrrev_i32_e32 v9, 31, v8
	v_ashrrev_i32_e32 v7, 8, v7
	v_add_u32_sdwa v8, v8, v9 dst_sel:DWORD dst_unused:UNUSED_PAD src0_sel:DWORD src1_sel:BYTE_3
	v_ashrrev_i32_e32 v8, 8, v8
	v_add_u32_e32 v6, v7, v6
	v_add_u32_e32 v8, v8, v6
	v_readlane_b32 s8, v252, 56
	v_lshlrev_b32_e32 v6, 8, v6
	v_lshlrev_b32_e32 v7, 8, v8
	v_mov_b32_e32 v9, s8
	ds_write2_b32 v9, v6, v7 offset1:1
	v_add_u32_e32 v9, 0xff, v4
	v_ashrrev_i32_e32 v10, 31, v9
	v_readlane_b32 s8, v252, 57
	v_add_u32_sdwa v9, v9, v10 dst_sel:DWORD dst_unused:UNUSED_PAD src0_sel:DWORD src1_sel:BYTE_3
	v_ashrrev_i32_e32 v9, 8, v9
	v_mov_b32_e32 v10, s8
	ds_write_b128 v10, v[2:5]
	v_add_u32_e32 v2, 0xff, v5
	v_ashrrev_i32_e32 v3, 31, v2
	v_add_u32_sdwa v2, v2, v3 dst_sel:DWORD dst_unused:UNUSED_PAD src0_sel:DWORD src1_sel:BYTE_3
	v_ashrrev_i32_e32 v2, 8, v2
	v_add_u32_e32 v3, v9, v8
	v_add_u32_e32 v19, v2, v3
	v_lshlrev_b32_e32 v8, 8, v3
	v_lshlrev_b32_e32 v9, 8, v19
	v_mov_b32_e32 v2, s10
	v_readlane_b32 s10, v252, 59
	s_add_u32 s8, s2, 0x556ec840
	ds_write_b128 v2, v[6:9]
	v_mov_b32_e32 v2, s10
	s_addc_u32 s9, s3, 0
	ds_write2_b32 v2, v8, v9 offset1:1
	v_mov_b64_e32 v[2:3], v[56:57]
	v_mov_b64_e32 v[4:5], v[58:59]
	v_mov_b64_e32 v[6:7], v[60:61]
	v_mov_b64_e32 v[8:9], v[62:63]
	v_mov_b64_e32 v[10:11], v[64:65]
	v_mov_b64_e32 v[12:13], v[66:67]
	v_mov_b64_e32 v[14:15], v[68:69]
	v_mov_b64_e32 v[16:17], v[70:71]
	v_readlane_b32 s8, v252, 60
	v_add_u32_e32 v20, 0xff, v14
	v_ashrrev_i32_e32 v21, 31, v20
	v_add_u32_sdwa v20, v20, v21 dst_sel:DWORD dst_unused:UNUSED_PAD src0_sel:DWORD src1_sel:BYTE_3
	v_add_u32_e32 v21, 0xff, v15
	v_ashrrev_i32_e32 v22, 31, v21
	v_ashrrev_i32_e32 v20, 8, v20
	v_add_u32_sdwa v21, v21, v22 dst_sel:DWORD dst_unused:UNUSED_PAD src0_sel:DWORD src1_sel:BYTE_3
	v_ashrrev_i32_e32 v21, 8, v21
	v_add_u32_e32 v19, v20, v19
	v_add_u32_e32 v22, v21, v19
	v_lshlrev_b32_e32 v20, 8, v19
	v_lshlrev_b32_e32 v21, 8, v22
	v_mov_b32_e32 v19, s8
	ds_write2_b32 v19, v20, v21 offset1:1
	v_add_u32_e32 v19, 0xff, v16
	v_ashrrev_i32_e32 v23, 31, v19
	v_readlane_b32 s8, v252, 61
	v_add_u32_sdwa v19, v19, v23 dst_sel:DWORD dst_unused:UNUSED_PAD src0_sel:DWORD src1_sel:BYTE_3
	v_ashrrev_i32_e32 v19, 8, v19
	v_mov_b32_e32 v23, s8
	ds_write_b128 v23, v[14:17]
	v_add_u32_e32 v14, 0xff, v17
	v_ashrrev_i32_e32 v15, 31, v14
	v_add_u32_sdwa v14, v14, v15 dst_sel:DWORD dst_unused:UNUSED_PAD src0_sel:DWORD src1_sel:BYTE_3
	v_ashrrev_i32_e32 v14, 8, v14
	v_add_u32_e32 v15, v19, v22
	v_add_u32_e32 v14, v14, v15
	v_readlane_b32 s8, v252, 62
	v_lshlrev_b32_e32 v22, 8, v15
	v_lshlrev_b32_e32 v23, 8, v14
	v_mov_b32_e32 v15, s8
	v_readlane_b32 s8, v252, 63
	ds_write_b128 v15, v[20:23]
	s_nop 0
	v_mov_b32_e32 v15, s8
	ds_write2_b32 v15, v22, v23 offset1:1
	v_add_u32_e32 v15, 0xff, v10
	v_ashrrev_i32_e32 v16, 31, v15
	v_add_u32_sdwa v15, v15, v16 dst_sel:DWORD dst_unused:UNUSED_PAD src0_sel:DWORD src1_sel:BYTE_3
	v_add_u32_e32 v16, 0xff, v11
	v_ashrrev_i32_e32 v17, 31, v16
	v_ashrrev_i32_e32 v15, 8, v15
	v_add_u32_sdwa v16, v16, v17 dst_sel:DWORD dst_unused:UNUSED_PAD src0_sel:DWORD src1_sel:BYTE_3
	v_ashrrev_i32_e32 v16, 8, v16
	v_add_u32_e32 v14, v15, v14
	v_add_u32_e32 v16, v16, v14
	v_readlane_b32 s8, v253, 0
	v_lshlrev_b32_e32 v14, 8, v14
	v_lshlrev_b32_e32 v15, 8, v16
	v_mov_b32_e32 v17, s8
	ds_write2_b32 v17, v14, v15 offset1:1
	v_add_u32_e32 v17, 0xff, v12
	v_ashrrev_i32_e32 v19, 31, v17
	v_readlane_b32 s8, v253, 1
	v_add_u32_sdwa v17, v17, v19 dst_sel:DWORD dst_unused:UNUSED_PAD src0_sel:DWORD src1_sel:BYTE_3
	v_ashrrev_i32_e32 v17, 8, v17
	v_mov_b32_e32 v19, s8
	ds_write_b128 v19, v[10:13]
	v_add_u32_e32 v10, 0xff, v13
	v_ashrrev_i32_e32 v11, 31, v10
	v_add_u32_sdwa v10, v10, v11 dst_sel:DWORD dst_unused:UNUSED_PAD src0_sel:DWORD src1_sel:BYTE_3
	v_ashrrev_i32_e32 v10, 8, v10
	v_add_u32_e32 v11, v17, v16
	v_add_u32_e32 v10, v10, v11
	v_readlane_b32 s8, v253, 2
	v_lshlrev_b32_e32 v16, 8, v11
	v_lshlrev_b32_e32 v17, 8, v10
	v_mov_b32_e32 v11, s8
	v_readlane_b32 s8, v253, 3
	ds_write_b128 v11, v[14:17]
	s_nop 0
	v_mov_b32_e32 v11, s8
	ds_write2_b32 v11, v16, v17 offset1:1
	v_add_u32_e32 v11, 0xff, v6
	v_ashrrev_i32_e32 v12, 31, v11
	v_add_u32_sdwa v11, v11, v12 dst_sel:DWORD dst_unused:UNUSED_PAD src0_sel:DWORD src1_sel:BYTE_3
	v_add_u32_e32 v12, 0xff, v7
	v_ashrrev_i32_e32 v13, 31, v12
	v_ashrrev_i32_e32 v11, 8, v11
	v_add_u32_sdwa v12, v12, v13 dst_sel:DWORD dst_unused:UNUSED_PAD src0_sel:DWORD src1_sel:BYTE_3
	v_ashrrev_i32_e32 v12, 8, v12
	v_add_u32_e32 v10, v11, v10
	v_add_u32_e32 v12, v12, v10
	v_readlane_b32 s8, v253, 4
	v_lshlrev_b32_e32 v10, 8, v10
	v_lshlrev_b32_e32 v11, 8, v12
	v_mov_b32_e32 v13, s8
	ds_write2_b32 v13, v10, v11 offset1:1
	v_add_u32_e32 v13, 0xff, v8
	v_ashrrev_i32_e32 v14, 31, v13
	v_readlane_b32 s8, v253, 5
	v_add_u32_sdwa v13, v13, v14 dst_sel:DWORD dst_unused:UNUSED_PAD src0_sel:DWORD src1_sel:BYTE_3
	v_ashrrev_i32_e32 v13, 8, v13
	v_mov_b32_e32 v14, s8
	ds_write_b128 v14, v[6:9]
	v_add_u32_e32 v6, 0xff, v9
	v_ashrrev_i32_e32 v7, 31, v6
	v_add_u32_sdwa v6, v6, v7 dst_sel:DWORD dst_unused:UNUSED_PAD src0_sel:DWORD src1_sel:BYTE_3
	v_ashrrev_i32_e32 v6, 8, v6
	v_add_u32_e32 v7, v13, v12
	v_add_u32_e32 v6, v6, v7
	v_readlane_b32 s8, v253, 6
	v_lshlrev_b32_e32 v12, 8, v7
	v_lshlrev_b32_e32 v13, 8, v6
	v_mov_b32_e32 v7, s8
	v_readlane_b32 s8, v253, 7
	ds_write_b128 v7, v[10:13]
	s_nop 0
	v_mov_b32_e32 v7, s8
	ds_write2_b32 v7, v12, v13 offset1:1
	v_add_u32_e32 v7, 0xff, v2
	v_ashrrev_i32_e32 v8, 31, v7
	v_add_u32_sdwa v7, v7, v8 dst_sel:DWORD dst_unused:UNUSED_PAD src0_sel:DWORD src1_sel:BYTE_3
	v_add_u32_e32 v8, 0xff, v3
	v_ashrrev_i32_e32 v9, 31, v8
	v_ashrrev_i32_e32 v7, 8, v7
	v_add_u32_sdwa v8, v8, v9 dst_sel:DWORD dst_unused:UNUSED_PAD src0_sel:DWORD src1_sel:BYTE_3
	v_ashrrev_i32_e32 v8, 8, v8
	v_add_u32_e32 v6, v7, v6
	v_add_u32_e32 v8, v8, v6
	v_readlane_b32 s8, v253, 8
	v_lshlrev_b32_e32 v6, 8, v6
	v_lshlrev_b32_e32 v7, 8, v8
	v_mov_b32_e32 v9, s8
	ds_write2_b32 v9, v6, v7 offset1:1
	v_add_u32_e32 v9, 0xff, v4
	v_ashrrev_i32_e32 v10, 31, v9
	v_readlane_b32 s8, v253, 9
	v_add_u32_sdwa v9, v9, v10 dst_sel:DWORD dst_unused:UNUSED_PAD src0_sel:DWORD src1_sel:BYTE_3
	v_ashrrev_i32_e32 v9, 8, v9
	v_mov_b32_e32 v10, s8
	ds_write_b128 v10, v[2:5]
	v_add_u32_e32 v2, 0xff, v5
	v_ashrrev_i32_e32 v3, 31, v2
	v_add_u32_sdwa v2, v2, v3 dst_sel:DWORD dst_unused:UNUSED_PAD src0_sel:DWORD src1_sel:BYTE_3
	v_lshrrev_b32_e32 v2, 8, v2
	v_add_u32_e32 v3, v9, v8
	v_add_u32_e32 v2, v2, v3
	v_readlane_b32 s8, v253, 10
	v_lshlrev_b32_e32 v9, 8, v2
	v_lshlrev_b32_e32 v8, 8, v3
	v_mov_b32_e32 v2, s8
	v_readlane_b32 s8, v253, 11
	ds_write_b32 v2, v8
	s_nop 0
	v_mov_b32_e32 v2, s8
	ds_write_b128 v2, v[6:9]
